# speedup vs baseline: 1.0088x; 1.0088x over previous
_Z8gemm_qkvPKDF16_S0_PKfS2_S2_PDF16_S3_S3_:
	s_load_dwordx8 s[12:19], s[0:1], 0x0
	s_load_dwordx8 s[4:11], s[0:1], 0x20
	s_mov_b32 s66, s2
	s_bitcmp0_b32 s2, 6
	s_mov_b64 s[0:1], -1
	s_cbranch_scc0 .LBB1_3
	s_and_b64 vcc, exec, s[0:1]
	s_cbranch_vccnz .LBB1_60

.LBB2_10:
	s_or_b64 exec, exec, s[4:5]
	v_and_b32_e32 v66, 15, v0
	v_lshl_or_b32 v66, v76, 6, v66
	v_lshl_add_u32 v67, v77, 8, 0
	v_mul_u32_u24_e32 v66, 0x210, v66
	v_add3_u32 v1, v67, v1, v66
	s_lshl_b64 s[4:5], s[10:11], 2
	s_waitcnt vmcnt(0)
	s_barrier
	ds_write_b128 v1, v[2:5]
	ds_write_b128 v1, v[6:9] offset:64
	ds_write_b128 v1, v[10:13] offset:128
	ds_write_b128 v1, v[14:17] offset:192
	ds_write_b128 v1, v[18:21] offset:8448
	ds_write_b128 v1, v[22:25] offset:8512
	ds_write_b128 v1, v[26:29] offset:8576
	ds_write_b128 v1, v[30:33] offset:8640
	ds_write_b128 v1, v[34:37] offset:16896
	ds_write_b128 v1, v[38:41] offset:16960
	ds_write_b128 v1, v[42:45] offset:17024
	ds_write_b128 v1, v[46:49] offset:17088
	ds_write_b128 v1, v[50:53] offset:25344
	ds_write_b128 v1, v[54:57] offset:25408
	ds_write_b128 v1, v[58:61] offset:25472
	ds_write_b128 v1, v[62:65] offset:25536
	v_and_b32_e32 v1, 31, v0
	s_add_u32 s0, s0, s4
	s_addc_u32 s1, s1, s5
	v_lshlrev_b32_e32 v8, 4, v1
	s_waitcnt lgkmcnt(0)
	s_barrier
	global_load_dwordx4 v[2:5], v8, s[0:1]
	v_lshrrev_b32_e32 v1, 5, v0
	v_or_b32_e32 v7, 0x200, v0
	v_or_b32_e32 v10, 0x600, v0
	v_or_b32_e32 v6, s8, v1
	v_lshrrev_b32_e32 v11, 5, v7
	s_movk_i32 s0, 0x210
	v_lshrrev_b32_e32 v12, 5, v10
	v_add_u32_e32 v50, 0, v8
	v_ashrrev_i32_e32 v7, 31, v6
	v_or_b32_e32 v10, s8, v11
	v_or_b32_e32 v18, 32, v6
	v_or_b32_e32 v20, s8, v12
	v_mad_u32_u24 v1, v1, s0, v50
	v_lshlrev_b64 v[42:43], 13, v[6:7]
	v_mad_u32_u24 v7, v11, s0, v50
	v_ashrrev_i32_e32 v11, 31, v10
	v_ashrrev_i32_e32 v19, 31, v18
	v_mad_u32_u24 v34, v12, s0, v50
	v_ashrrev_i32_e32 v21, 31, v20
	v_lshlrev_b64 v[44:45], 13, v[10:11]
	ds_read_b128 v[10:13], v1
	ds_read_b128 v[14:17], v1 offset:16896
	v_add_u32_e32 v38, 0x8400, v1
	s_add_u32 s2, s2, s4
	v_add_u32_e32 v51, 0x4200, v1
	v_lshlrev_b64 v[46:47], 13, v[18:19]
	v_lshlrev_b64 v[48:49], 13, v[20:21]
	ds_read_b128 v[18:21], v1 offset:33792
	ds_read_b128 v[22:25], v1 offset:50688
	ds_read_b128 v[26:29], v7
	ds_read_b128 v[30:33], v51 offset:50688
	ds_read_b128 v[34:37], v34
	ds_read_b128 v[38:41], v38 offset:50688
	v_mov_b32_e32 v9, 0
	s_addc_u32 s3, s3, s5
	v_lshl_add_u64 v[8:9], s[2:3], 0, v[8:9]
	v_lshl_add_u64 v[42:43], v[8:9], 0, v[42:43]
	v_lshl_add_u64 v[44:45], v[8:9], 0, v[44:45]
	v_lshl_add_u64 v[46:47], v[8:9], 0, v[46:47]
	v_lshl_add_u64 v[48:49], v[8:9], 0, v[48:49]
	v_or_b32_e32 v7, 0xa00, v0
	v_lshrrev_b32_e32 v7, 5, v7
	v_add_u32_e32 v1, 0xc600, v1
	s_waitcnt vmcnt(0) lgkmcnt(7)
	v_pk_add_f32 v[12:13], v[4:5], v[12:13]
	v_pk_add_f32 v[10:11], v[2:3], v[10:11]
	s_waitcnt lgkmcnt(3)
	v_pk_add_f32 v[28:29], v[4:5], v[28:29]
	v_pk_add_f32 v[26:27], v[2:3], v[26:27]
	v_pk_add_f32 v[16:17], v[4:5], v[16:17]
	v_pk_add_f32 v[14:15], v[2:3], v[14:15]
	s_waitcnt lgkmcnt(1)
	v_pk_add_f32 v[36:37], v[4:5], v[36:37]
	v_pk_add_f32 v[34:35], v[2:3], v[34:35]
	global_store_dwordx4 v[42:43], v[10:13], off nt
	global_store_dwordx4 v[44:45], v[26:29], off nt
	global_store_dwordx4 v[46:47], v[14:17], off nt
	global_store_dwordx4 v[48:49], v[34:37], off nt
	v_or_b32_e32 v10, 64, v6
	v_ashrrev_i32_e32 v11, 31, v10
	v_lshlrev_b64 v[14:15], 13, v[10:11]
	v_mad_u32_u24 v10, v7, s0, v50
	ds_read_b128 v[10:13], v10
	v_pk_add_f32 v[20:21], v[4:5], v[20:21]
	v_pk_add_f32 v[18:19], v[2:3], v[18:19]
	v_lshl_add_u64 v[14:15], v[8:9], 0, v[14:15]
	global_store_dwordx4 v[14:15], v[18:21], off nt
	ds_read_b128 v[14:17], v1 offset:50688
	s_waitcnt lgkmcnt(1)
	v_pk_add_f32 v[12:13], v[4:5], v[12:13]
	v_or_b32_e32 v18, s8, v7
	v_ashrrev_i32_e32 v19, 31, v18
	v_lshlrev_b64 v[18:19], 13, v[18:19]
	v_pk_add_f32 v[10:11], v[2:3], v[10:11]
	v_lshl_add_u64 v[18:19], v[8:9], 0, v[18:19]
	v_or_b32_e32 v1, 0xe00, v0
	global_store_dwordx4 v[18:19], v[10:13], off nt
	v_or_b32_e32 v18, 0x60, v6
	v_lshrrev_b32_e32 v1, 5, v1
	v_ashrrev_i32_e32 v19, 31, v18
	v_mad_u32_u24 v7, v1, s0, v50
	v_pk_add_f32 v[10:11], v[2:3], v[22:23]
	v_lshlrev_b64 v[22:23], 13, v[18:19]
	ds_read_b128 v[18:21], v7
	v_pk_add_f32 v[12:13], v[4:5], v[24:25]
	v_lshl_add_u64 v[22:23], v[8:9], 0, v[22:23]
	global_store_dwordx4 v[22:23], v[10:13], off nt
	v_or_b32_e32 v22, s8, v1
	v_ashrrev_i32_e32 v23, 31, v22
	v_lshlrev_b64 v[22:23], 13, v[22:23]
	s_waitcnt lgkmcnt(0)
	v_pk_add_f32 v[20:21], v[4:5], v[20:21]
	v_pk_add_f32 v[18:19], v[2:3], v[18:19]
	v_lshl_add_u64 v[22:23], v[8:9], 0, v[22:23]
	global_store_dwordx4 v[22:23], v[18:21], off nt
	v_or_b32_e32 v22, 0x80, v6
	v_ashrrev_i32_e32 v23, 31, v22
	v_or_b32_e32 v1, 0x1200, v0
	v_add_u32_e32 v7, 0xc600, v51
	v_lshlrev_b64 v[22:23], 13, v[22:23]
	v_lshrrev_b32_e32 v1, 5, v1
	ds_read_b128 v[10:13], v7 offset:50688
	v_pk_add_f32 v[20:21], v[4:5], v[32:33]
	v_pk_add_f32 v[18:19], v[2:3], v[30:31]
	v_lshl_add_u64 v[22:23], v[8:9], 0, v[22:23]
	v_mad_u32_u24 v7, v1, s0, v50
	global_store_dwordx4 v[22:23], v[18:21], off nt
	ds_read_b128 v[18:21], v7
	v_or_b32_e32 v7, 0x1600, v0
	v_or_b32_e32 v26, s8, v1
	v_lshrrev_b32_e32 v7, 5, v7
	v_ashrrev_i32_e32 v27, 31, v26
	v_mad_u32_u24 v22, v7, s0, v50
	v_lshlrev_b64 v[26:27], 13, v[26:27]
	ds_read_b128 v[22:25], v22
	s_waitcnt lgkmcnt(1)
	v_pk_add_f32 v[20:21], v[4:5], v[20:21]
	v_pk_add_f32 v[18:19], v[2:3], v[18:19]
	v_lshl_add_u64 v[26:27], v[8:9], 0, v[26:27]
	global_store_dwordx4 v[26:27], v[18:21], off nt
	v_or_b32_e32 v26, 0xa0, v6
	v_ashrrev_i32_e32 v27, 31, v26
	v_lshlrev_b64 v[26:27], 13, v[26:27]
	v_pk_add_f32 v[20:21], v[4:5], v[40:41]
	v_pk_add_f32 v[18:19], v[2:3], v[38:39]
	v_lshl_add_u64 v[26:27], v[8:9], 0, v[26:27]
	global_store_dwordx4 v[26:27], v[18:21], off nt
	v_or_b32_e32 v1, 0x1a00, v0
	v_lshrrev_b32_e32 v1, 5, v1
	s_waitcnt lgkmcnt(0)
	v_pk_add_f32 v[18:19], v[2:3], v[22:23]
	v_or_b32_e32 v22, s8, v7
	v_ashrrev_i32_e32 v23, 31, v22
	v_lshlrev_b64 v[22:23], 13, v[22:23]
	v_pk_add_f32 v[20:21], v[4:5], v[24:25]
	v_lshl_add_u64 v[22:23], v[8:9], 0, v[22:23]
	global_store_dwordx4 v[22:23], v[18:21], off nt
	v_pk_add_f32 v[16:17], v[4:5], v[16:17]
	v_pk_add_f32 v[14:15], v[2:3], v[14:15]
	v_or_b32_e32 v18, 0xc0, v6
	v_ashrrev_i32_e32 v19, 31, v18
	v_lshlrev_b64 v[18:19], 13, v[18:19]
	v_lshl_add_u64 v[18:19], v[8:9], 0, v[18:19]
	v_mad_u32_u24 v7, v1, s0, v50
	v_or_b32_e32 v0, 0x1e00, v0
	global_store_dwordx4 v[18:19], v[14:17], off nt
	ds_read_b128 v[14:17], v7
	v_lshrrev_b32_e32 v7, 5, v0
	v_mad_u32_u24 v0, v7, s0, v50
	ds_read_b128 v[18:21], v0
	v_or_b32_e32 v0, s8, v1
	v_ashrrev_i32_e32 v1, 31, v0
	v_lshlrev_b64 v[0:1], 13, v[0:1]
	s_waitcnt lgkmcnt(1)
	v_pk_add_f32 v[16:17], v[4:5], v[16:17]
	v_pk_add_f32 v[14:15], v[2:3], v[14:15]
	v_lshl_add_u64 v[0:1], v[8:9], 0, v[0:1]
	global_store_dwordx4 v[0:1], v[14:17], off nt
	v_or_b32_e32 v0, 0xe0, v6
	v_ashrrev_i32_e32 v1, 31, v0
	v_lshlrev_b64 v[0:1], 13, v[0:1]
	v_pk_add_f32 v[12:13], v[4:5], v[12:13]
	v_pk_add_f32 v[10:11], v[2:3], v[10:11]
	v_lshl_add_u64 v[0:1], v[8:9], 0, v[0:1]
	global_store_dwordx4 v[0:1], v[10:13], off nt
	v_add_u32_e32 v0, s8, v7
	v_ashrrev_i32_e32 v1, 31, v0
	v_lshlrev_b64 v[0:1], 13, v[0:1]
	s_waitcnt lgkmcnt(0)
	v_pk_add_f32 v[4:5], v[4:5], v[20:21]
	v_pk_add_f32 v[2:3], v[2:3], v[18:19]
	v_lshl_add_u64 v[0:1], v[8:9], 0, v[0:1]
	global_store_dwordx4 v[0:1], v[2:5], off nt
	s_endpgm

.LBB3_12:
	v_exp_f32_e32 v48, v48
	v_exp_f32_e32 v49, v49
	v_mfma_f32_32x32x16_f16 v[112:127], a[192:195], a[128:131], v[16:31]
	ds_read_b64_tr_b16 v[180:181], v225 offset:0
	v_cvt_pk_f16_f32 v164, v128, v129
	v_exp_f32_e32 v50, v50
	v_exp_f32_e32 v51, v51
	v_mfma_f32_32x32x16_f16 v[96:111], a[192:195], a[160:163], v[0:15]
	ds_read_b64_tr_b16 v[182:183], v225 offset:0x800
	v_cvt_pk_f16_f32 v165, v130, v131
	v_mfma_f32_32x32x16_f16 v[80:95], a[224:227], a[128:131], v[16:31]
	ds_read_b64_tr_b16 v[184:185], v225 offset:0x200
	v_exp_f32_e32 v238, v52
	v_exp_f32_e32 v239, v53
	v_cvt_pk_f16_f32 v166, v132, v133
	v_mfma_f32_32x32x16_f16 v[64:79], a[224:227], a[160:163], v[0:15]
	ds_read_b64_tr_b16 v[186:187], v225 offset:0xa00
	ds_read_b64_tr_b16 v[176:177], v225 offset:0x400
	v_exp_f32_e32 v244, v54
	v_exp_f32_e32 v245, v55
	v_cvt_pk_f16_f32 v167, v134, v135
	v_exp_f32_e32 v198, v56
	v_exp_f32_e32 v199, v57
	v_mfma_f32_32x32x16_f16 v[112:127], a[196:199], a[132:135], v[112:127]
	ds_read_b64_tr_b16 v[178:179], v225 offset:0xc00
	v_cvt_pk_f16_f32 v128, v136, v137
	v_exp_f32_e32 v232, v58
	v_exp_f32_e32 v233, v59
	v_mfma_f32_32x32x16_f16 v[96:111], a[196:199], a[164:167], v[96:111]
	ds_read_b64_tr_b16 v[188:189], v225 offset:0x600
	v_cvt_pk_f16_f32 v129, v138, v139
	v_exp_f32_e32 v234, v60
	v_exp_f32_e32 v235, v61
	v_mfma_f32_32x32x16_f16 v[80:95], a[228:231], a[132:135], v[80:95]
	ds_read_b64_tr_b16 v[190:191], v225 offset:0xe00
	v_cvt_pk_f16_f32 v130, v140, v141
	v_mfma_f32_32x32x16_f16 v[64:79], a[228:231], a[164:167], v[64:79]
	ds_read_b64_tr_b16 v[172:173], v225 offset:0x1000
	v_exp_f32_e32 v236, v62
	v_exp_f32_e32 v237, v63
	ds_read_b64_tr_b16 v[174:175], v225 offset:0x1800
	v_cvt_pk_f16_f32 v131, v142, v143
	v_exp_f32_e32 v141, v32
	v_exp_f32_e32 v142, v33
	v_mfma_f32_32x32x16_f16 v[112:127], a[200:203], a[136:139], v[112:127]
	ds_read_b64_tr_b16 v[168:169], v225 offset:0x1200
	v_cvt_pk_f16_f32 v192, v144, v145
	v_exp_f32_e32 v143, v34
	v_mfma_f32_32x32x16_f16 v[96:111], a[200:203], a[168:171], v[96:111]
	ds_read_b64_tr_b16 v[170:171], v225 offset:0x1a00
	v_exp_f32_e32 v246, v35
	v_cvt_pk_f16_f32 v193, v146, v147
	v_mfma_f32_32x32x16_f16 v[80:95], a[232:235], a[136:139], v[80:95]
	ds_read_b64_tr_b16 v[160:161], v225 offset:0x1400
	v_exp_f32_e32 v247, v36
	v_exp_f32_e32 v248, v37
	v_cvt_pk_f16_f32 v194, v148, v149
	v_mfma_f32_32x32x16_f16 v[64:79], a[232:235], a[168:171], v[64:79]
	ds_read_b64_tr_b16 v[162:163], v225 offset:0x1c00
	ds_read_b64_tr_b16 v[136:137], v225 offset:0x1600
	v_exp_f32_e32 v249, v38
	v_exp_f32_e32 v250, v39
	v_cvt_pk_f16_f32 v195, v150, v151
	v_exp_f32_e32 v148, v40
	v_exp_f32_e32 v149, v41
	v_mfma_f32_32x32x16_f16 v[112:127], a[204:207], a[140:143], v[112:127]
	ds_read_b64_tr_b16 v[138:139], v225 offset:0x1e00
	v_cvt_pk_f16_f32 v144, v152, v153
	v_exp_f32_e32 v150, v42
	v_exp_f32_e32 v151, v43
	v_mfma_f32_32x32x16_f16 v[96:111], a[204:207], a[172:175], v[96:111]
	ds_read_b64_tr_b16 v[132:133], v225 offset:0x2000
	v_cvt_pk_f16_f32 v145, v154, v155
	v_exp_f32_e32 v152, v44
	v_exp_f32_e32 v153, v45
	v_mfma_f32_32x32x16_f16 v[80:95], a[236:239], a[140:143], v[80:95]
	ds_read_b64_tr_b16 v[134:135], v225 offset:0x2800
	v_cvt_pk_f16_f32 v146, v156, v157
	v_mfma_f32_32x32x16_f16 v[64:79], a[236:239], a[172:175], v[64:79]
	ds_read_b64_tr_b16 v[60:61], v225 offset:0x2200
	v_exp_f32_e32 v154, v46
	v_exp_f32_e32 v155, v47
	ds_read_b64_tr_b16 v[62:63], v225 offset:0x2a00
	v_cvt_pk_f16_f32 v147, v158, v159
	s_mov_b32 s0, s33
	v_mfma_f32_32x32x16_f16 v[112:127], a[208:211], a[144:147], v[112:127]
	ds_read_b64_tr_b16 v[56:57], v225 offset:0x2400
	v_cvt_pk_f16_f32 v52, v48, v49
	v_add_f32_e32 v32, v241, v48
	v_add_f32_e32 v33, v240, v49
	s_add_i32 s31, s36, s12
	s_add_i32 s24, s31, 0x10000
	s_mov_b32 s1, s24
	v_mfma_f32_32x32x16_f16 v[96:111], a[208:211], a[176:179], v[96:111]
	ds_read_b64_tr_b16 v[58:59], v225 offset:0x2c00
	v_cvt_pk_f16_f32 v53, v50, v51
	v_add_f32_e32 v32, v32, v50
	v_add_f32_e32 v33, v33, v51
	s_mov_b32 s34, s41
	v_mfma_f32_32x32x16_f16 v[80:95], a[240:243], a[144:147], v[80:95]
	ds_read_b64_tr_b16 v[48:49], v225 offset:0x2600
	v_cvt_pk_f16_f32 v54, v238, v239
	v_add_f32_e32 v32, v32, v238
	v_add_f32_e32 v33, v33, v239
	s_add_i32 s35, s31, 0x10400
	v_mfma_f32_32x32x16_f16 v[64:79], a[240:243], a[176:179], v[64:79]
	ds_read_b64_tr_b16 v[50:51], v225 offset:0x2e00
	ds_read_b64_tr_b16 v[44:45], v225 offset:0x3000
	v_cvt_pk_f16_f32 v55, v244, v245
	v_add_f32_e32 v32, v32, v244
	v_add_f32_e32 v33, v33, v245
	s_mov_b32 s91, s43
	v_mfma_f32_32x32x16_f16 v[112:127], a[212:215], a[148:151], v[112:127]
	ds_read_b64_tr_b16 v[46:47], v225 offset:0x3800
	v_add_f32_e32 v32, v32, v198
	v_add_f32_e32 v33, v33, v199
	s_add_i32 s30, s31, 0x10800
	s_mov_b32 s92, s30
	v_mfma_f32_32x32x16_f16 v[96:111], a[212:215], a[180:183], v[96:111]
	ds_read_b64_tr_b16 v[40:41], v225 offset:0x3200
	v_add_f32_e32 v32, v32, v232
	v_add_f32_e32 v33, v33, v233
	s_mov_b32 s93, s45
	v_mfma_f32_32x32x16_f16 v[80:95], a[244:247], a[148:151], v[80:95]
	ds_read_b64_tr_b16 v[42:43], v225 offset:0x3a00
	v_add_f32_e32 v32, v32, v234
	v_add_f32_e32 v33, v33, v235
	s_add_i32 s94, s31, 0x10c00
	v_mfma_f32_32x32x16_f16 v[64:79], a[244:247], a[180:183], v[64:79]
	ds_read_b64_tr_b16 v[36:37], v225 offset:0x3400
	ds_read_b64_tr_b16 v[38:39], v225 offset:0x3c00
	v_add_f32_e32 v156, v32, v236
	v_add_f32_e32 v157, v33, v237
	s_mov_b32 s95, s47
	v_mfma_f32_32x32x16_f16 v[112:127], a[216:219], a[152:155], v[112:127]
	ds_read_b64_tr_b16 v[32:33], v225 offset:0x3600
	v_cvt_pk_f16_f32 v140, v141, v142
	v_add_f32_e32 v158, v242, v141
	v_add_f32_e32 v142, v243, v142
	s_add_i32 s96, s31, 0xc000
	v_mfma_f32_32x32x16_f16 v[96:111], a[216:219], a[184:187], v[96:111]
	ds_read_b64_tr_b16 v[34:35], v225 offset:0x3e00
	v_cvt_pk_f16_f32 v141, v143, v246
	v_add_f32_e32 v143, v158, v143
	v_add_f32_e32 v158, v142, v246
	v_mfma_f32_32x32x16_f16 v[80:95], a[248:251], a[152:155], v[80:95]
	s_mov_b32 s97, s49
	v_cvt_pk_f16_f32 v142, v247, v248
	v_add_f32_e32 v159, v143, v247
	v_add_f32_e32 v158, v158, v248
	v_mfma_f32_32x32x16_f16 v[64:79], a[248:251], a[184:187], v[64:79]
	s_add_i32 s98, s31, 0xc080
	v_cvt_pk_f16_f32 v143, v249, v250
	v_add_f32_e32 v159, v159, v249
	v_add_f32_e32 v158, v158, v250
	v_mfma_f32_32x32x16_f16 v[112:127], a[220:223], a[156:159], v[112:127]
	s_mov_b32 s99, s51
	v_add_f32_e32 v159, v159, v148
	v_add_f32_e32 v158, v158, v149
	v_mfma_f32_32x32x16_f16 v[96:111], a[220:223], a[188:191], v[96:111]
	s_add_i32 vcc_lo, s31, 0xc800
	v_add_f32_e32 v159, v159, v150
	v_add_f32_e32 v158, v158, v151
	v_mfma_f32_32x32x16_f16 v[80:95], a[252:255], a[156:159], v[80:95]
	s_mov_b32 vcc_hi, s53
	v_add_f32_e32 v159, v159, v152
	v_add_f32_e32 v158, v158, v153
	v_mfma_f32_32x32x16_f16 v[64:79], a[252:255], a[188:191], v[64:79]
	s_add_i32 s80, s31, 0xc880
	v_add_f32_e32 v159, v159, v154
	v_add_f32_e32 v158, v158, v155
	s_nop 4
	v_add_f32_e32 v156, v156, v157
	s_waitcnt vmcnt(0) lgkmcnt(0)
	s_barrier
	v_mov_b32_e32 v157, v156
	s_nop 1
	v_permlane32_swap_b32_e32 v156, v157
	v_add_f32_e32 v156, v156, v157
	v_add_f32_e32 v197, v197, v156
	v_add_f32_e32 v156, v159, v158
	v_mov_b32_e32 v157, v156
	s_nop 1
	v_permlane32_swap_b32_e32 v156, v157
	v_add_f32_e32 v156, v156, v157
	v_add_f32_e32 v196, v196, v156
	s_nop 1
	v_mfma_f32_32x32x16_f16 a[0:15], v[180:183], v[164:167], a[0:15]
	s_mov_b32 m0, s0
	s_nop 0
	buffer_load_dwordx4 v211, s[16:19], s1 offen lds
	v_mfma_f32_32x32x16_f16 a[16:31], v[180:183], v[192:195], a[16:31]
	s_mov_b32 m0, s34
	s_nop 0
	buffer_load_dwordx4 v212, s[16:19], s35 offen lds
	ds_read_b128 a[192:195], v221 offset:0
	v_mfma_f32_32x32x16_f16 a[32:47], v[184:187], v[164:167], a[32:47]
	s_mov_b32 m0, s91
	s_nop 0
	buffer_load_dwordx4 v211, s[16:19], s92 offen lds
	ds_read_b128 a[196:199], v222 offset:0
	v_mfma_f32_32x32x16_f16 a[48:63], v[184:187], v[192:195], a[48:63]
	s_mov_b32 m0, s93
	s_nop 0
	buffer_load_dwordx4 v212, s[16:19], s94 offen lds
	ds_read_b128 a[200:203], v223 offset:0
	v_mfma_f32_32x32x16_f16 a[64:79], v[176:179], v[164:167], a[64:79]
	s_mov_b32 m0, s95
	s_nop 0
	buffer_load_dwordx4 v213, s[20:23], s96 offen lds
	ds_read_b128 a[204:207], v224 offset:0
	v_mfma_f32_32x32x16_f16 a[80:95], v[176:179], v[192:195], a[80:95]
	s_mov_b32 m0, s97
	s_nop 0
	buffer_load_dwordx4 v213, s[20:23], s98 offen lds
	ds_read_b128 a[208:211], v221 offset:128
	v_mfma_f32_32x32x16_f16 a[96:111], v[188:191], v[164:167], a[96:111]
	s_mov_b32 m0, s99
	s_nop 0
	buffer_load_dwordx4 v213, s[20:23], vcc_lo offen lds
	ds_read_b128 a[212:215], v222 offset:128
	v_mfma_f32_32x32x16_f16 a[112:127], v[188:191], v[192:195], a[112:127]
	s_mov_b32 m0, vcc_hi
	s_nop 0
	buffer_load_dwordx4 v213, s[20:23], s80 offen lds
	ds_read_b128 a[216:219], v223 offset:128
	v_mfma_f32_32x32x16_f16 a[0:15], v[172:175], v[128:131], a[0:15]
	ds_read_b128 a[220:223], v224 offset:128
	v_max3_f32 v156, v112, v113, v80
	v_max3_f32 v157, v114, v115, v81
	v_max3_f32 v156, v156, v82, v83
	v_mfma_f32_32x32x16_f16 a[16:31], v[172:175], v[144:147], a[16:31]
	ds_read_b128 a[224:227], v221 offset:8192
	v_max3_f32 v156, v156, v116, v117
	v_max3_f32 v157, v157, v118, v119
	v_max3_f32 v156, v156, v84, v85
	v_max3_f32 v157, v157, v86, v87
	v_mfma_f32_32x32x16_f16 a[32:47], v[168:171], v[128:131], a[32:47]
	ds_read_b128 a[228:231], v222 offset:8192
	v_max3_f32 v156, v156, v120, v121
	v_max3_f32 v157, v157, v122, v123
	v_max3_f32 v156, v156, v88, v89
	v_max3_f32 v157, v157, v90, v91
	v_mfma_f32_32x32x16_f16 a[48:63], v[168:171], v[144:147], a[48:63]
	ds_read_b128 a[232:235], v223 offset:8192
	v_max3_f32 v156, v156, v124, v125
	v_max3_f32 v157, v157, v126, v127
	v_max3_f32 v156, v156, v92, v93
	v_max3_f32 v157, v157, v94, v95
	v_mfma_f32_32x32x16_f16 a[64:79], v[160:163], v[128:131], a[64:79]
	ds_read_b128 a[236:239], v224 offset:8192
	v_max3_f32 v158, v96, v97, v64
	v_max3_f32 v159, v98, v99, v65
	v_max3_f32 v158, v158, v66, v67
	v_mfma_f32_32x32x16_f16 a[80:95], v[160:163], v[144:147], a[80:95]
	ds_read_b128 a[240:243], v221 offset:8320
	v_max3_f32 v158, v158, v100, v101
	v_max3_f32 v159, v159, v102, v103
	v_max3_f32 v158, v158, v68, v69
	v_max3_f32 v159, v159, v70, v71
	v_mfma_f32_32x32x16_f16 a[96:111], v[136:139], v[128:131], a[96:111]
	ds_read_b128 a[244:247], v222 offset:8320
	v_max3_f32 v128, v158, v104, v105
	v_max3_f32 v129, v159, v106, v107
	v_max3_f32 v128, v128, v72, v73
	v_max3_f32 v129, v129, v74, v75
	v_mfma_f32_32x32x16_f16 a[112:127], v[136:139], v[144:147], a[112:127]
	ds_read_b128 a[248:251], v223 offset:8320
	v_max3_f32 v128, v128, v108, v109
	v_max3_f32 v129, v129, v110, v111
	v_max3_f32 v128, v128, v76, v77
	v_max3_f32 v130, v129, v78, v79
	v_mfma_f32_32x32x16_f16 a[0:15], v[132:135], v[52:55], a[0:15]
	ds_read_b128 a[252:255], v224 offset:8320
	v_max_f32_e32 v129, v156, v157
	v_mov_b32_e32 v131, v129
	s_nop 1
	v_permlane32_swap_b32_e32 v129, v131
	v_max_f32_e32 v129, v129, v131
	v_mfma_f32_32x32x16_f16 a[16:31], v[132:135], v[140:143], a[16:31]
	v_max_f32_e32 v128, v128, v130
	v_mov_b32_e32 v130, v128
	s_nop 1
	v_permlane32_swap_b32_e32 v128, v130
	v_max_f32_e32 v128, v128, v130
	v_max_f32_e32 v130, v129, v129
	v_max_f32_e32 v131, v128, v128
	v_max_f32_e32 v130, v130, v131
	v_mfma_f32_32x32x16_f16 a[32:47], v[60:63], v[52:55], a[32:47]
	v_cmp_lt_f32_e32 vcc, s79, v130
	s_cmp_lg_u64 vcc, 0
	s_cselect_b64 s[0:1], -1, 0
	s_cbranch_vccnz .LBB3_17
.LBB3_13:
	v_cvt_pk_f16_f32 v156, v198, v199
	v_cvt_pk_f16_f32 v157, v232, v233
	v_cvt_pk_f16_f32 v158, v234, v235
	v_cvt_pk_f16_f32 v159, v236, v237
	v_cvt_pk_f16_f32 v160, v148, v149
	v_cvt_pk_f16_f32 v161, v150, v151
	v_cvt_pk_f16_f32 v162, v152, v153
	v_cvt_pk_f16_f32 v163, v154, v155
	v_exp_f32_e32 v128, v112
	v_exp_f32_e32 v129, v113
	v_mfma_f32_32x32x16_f16 a[48:63], v[60:63], v[140:143], a[48:63]
	v_exp_f32_e32 v130, v114
	v_exp_f32_e32 v131, v115
	v_mfma_f32_32x32x16_f16 a[64:79], v[56:59], v[52:55], a[64:79]
	v_add_f32_e32 v60, v201, v128
	v_add_f32_e32 v61, v201, v129
	v_exp_f32_e32 v132, v116
	v_exp_f32_e32 v133, v117
	v_exp_f32_e32 v134, v118
	v_mfma_f32_32x32x16_f16 a[80:95], v[56:59], v[140:143], a[80:95]
	v_add_f32_e32 v56, v60, v130
	v_add_f32_e32 v57, v61, v131
	v_exp_f32_e32 v135, v119
	v_exp_f32_e32 v136, v120
	v_mfma_f32_32x32x16_f16 a[96:111], v[48:51], v[52:55], a[96:111]
	v_add_f32_e32 v52, v56, v132
	v_add_f32_e32 v53, v57, v133
	v_add_f32_e32 v52, v52, v134
	v_exp_f32_e32 v137, v121
	v_exp_f32_e32 v138, v122
	v_exp_f32_e32 v139, v123
	v_mfma_f32_32x32x16_f16 a[112:127], v[48:51], v[140:143], a[112:127]
	v_add_f32_e32 v48, v53, v135
	v_add_f32_e32 v49, v52, v136
	v_exp_f32_e32 v140, v124
	v_exp_f32_e32 v141, v125
	v_mfma_f32_32x32x16_f16 a[0:15], v[44:47], v[156:159], a[0:15]
	v_add_f32_e32 v48, v48, v137
	v_add_f32_e32 v49, v49, v138
	v_add_f32_e32 v48, v48, v139
	v_exp_f32_e32 v142, v126
	v_exp_f32_e32 v143, v127
	v_exp_f32_e32 v144, v96
	v_mfma_f32_32x32x16_f16 a[16:31], v[44:47], v[160:163], a[16:31]
	v_add_f32_e32 v44, v49, v140
	v_add_f32_e32 v45, v48, v141
	v_exp_f32_e32 v145, v97
	v_exp_f32_e32 v146, v98
	v_mfma_f32_32x32x16_f16 a[32:47], v[40:43], v[156:159], a[32:47]
	v_add_f32_e32 v239, v44, v142
	v_add_f32_e32 v238, v45, v143
	v_add_f32_e32 v44, v201, v144
	v_exp_f32_e32 v147, v99
	v_exp_f32_e32 v148, v100
	v_exp_f32_e32 v149, v101
	v_mfma_f32_32x32x16_f16 a[48:63], v[40:43], v[160:163], a[48:63]
	v_add_f32_e32 v40, v201, v145
	v_add_f32_e32 v41, v44, v146
	v_exp_f32_e32 v150, v102
	v_exp_f32_e32 v151, v103
	v_mfma_f32_32x32x16_f16 a[64:79], v[36:39], v[156:159], a[64:79]
	v_add_f32_e32 v40, v40, v147
	v_add_f32_e32 v41, v41, v148
	v_add_f32_e32 v40, v40, v149
	v_exp_f32_e32 v152, v104
	v_exp_f32_e32 v153, v105
	v_exp_f32_e32 v154, v106
	v_mfma_f32_32x32x16_f16 a[80:95], v[36:39], v[160:163], a[80:95]
	v_add_f32_e32 v36, v41, v150
	v_add_f32_e32 v37, v40, v151
	v_mfma_f32_32x32x16_f16 a[96:111], v[32:35], v[156:159], a[96:111]
	v_exp_f32_e32 v155, v107
	v_exp_f32_e32 v156, v108
	v_add_f32_e32 v36, v36, v152
	v_add_f32_e32 v37, v37, v153
	v_add_f32_e32 v36, v36, v154
	v_exp_f32_e32 v157, v109
	v_exp_f32_e32 v158, v110
	v_exp_f32_e32 v159, v111
	v_mfma_f32_32x32x16_f16 a[112:127], v[32:35], v[160:163], a[112:127]
	v_add_f32_e32 v32, v37, v155
	v_add_f32_e32 v33, v36, v156
	s_andn2_b64 vcc, exec, s[0:1]
	v_add_f32_e32 v32, v32, v157
	v_add_f32_e32 v240, v33, v158
	s_nop 0
	v_add_f32_e32 v241, v32, v159
	s_cbranch_vccz .LBB3_18
.LBB3_14:
	s_waitcnt lgkmcnt(0)
	v_exp_f32_e32 v80, v80
	v_exp_f32_e32 v81, v81
	v_mfma_f32_32x32x16_f16 v[112:127], a[192:195], a[128:131], v[16:31]
	ds_read_b64_tr_b16 v[180:181], v210 offset:0
	v_cvt_pk_f16_f32 v164, v128, v129
	v_exp_f32_e32 v82, v82
	v_exp_f32_e32 v83, v83
	v_mfma_f32_32x32x16_f16 v[96:111], a[192:195], a[160:163], v[0:15]
	ds_read_b64_tr_b16 v[182:183], v210 offset:0x800
	v_cvt_pk_f16_f32 v165, v130, v131
	v_mfma_f32_32x32x16_f16 v[48:63], a[224:227], a[128:131], v[16:31]
	ds_read_b64_tr_b16 v[184:185], v210 offset:0x200
	v_exp_f32_e32 v242, v84
	v_exp_f32_e32 v243, v85
	v_cvt_pk_f16_f32 v166, v132, v133
	v_mfma_f32_32x32x16_f16 v[32:47], a[224:227], a[160:163], v[0:15]
	ds_read_b64_tr_b16 v[186:187], v210 offset:0xa00
	ds_read_b64_tr_b16 v[176:177], v210 offset:0x400
	v_exp_f32_e32 v244, v86
	v_exp_f32_e32 v245, v87
	v_cvt_pk_f16_f32 v167, v134, v135
	v_exp_f32_e32 v198, v88
	v_exp_f32_e32 v199, v89
	v_mfma_f32_32x32x16_f16 v[112:127], a[196:199], a[132:135], v[112:127]
	ds_read_b64_tr_b16 v[178:179], v210 offset:0xc00
	v_cvt_pk_f16_f32 v128, v136, v137
	v_exp_f32_e32 v232, v90
	v_exp_f32_e32 v233, v91
	v_mfma_f32_32x32x16_f16 v[96:111], a[196:199], a[164:167], v[96:111]
	ds_read_b64_tr_b16 v[188:189], v210 offset:0x600
	v_cvt_pk_f16_f32 v129, v138, v139
	v_exp_f32_e32 v234, v92
	v_exp_f32_e32 v235, v93
	v_mfma_f32_32x32x16_f16 v[48:63], a[228:231], a[132:135], v[48:63]
	ds_read_b64_tr_b16 v[190:191], v210 offset:0xe00
	v_cvt_pk_f16_f32 v130, v140, v141
	v_mfma_f32_32x32x16_f16 v[32:47], a[228:231], a[164:167], v[32:47]
	ds_read_b64_tr_b16 v[172:173], v210 offset:0x1000
	v_exp_f32_e32 v236, v94
	v_exp_f32_e32 v237, v95
	ds_read_b64_tr_b16 v[174:175], v210 offset:0x1800
	v_cvt_pk_f16_f32 v131, v142, v143
	v_exp_f32_e32 v141, v64
	v_exp_f32_e32 v142, v65
	v_mfma_f32_32x32x16_f16 v[112:127], a[200:203], a[136:139], v[112:127]
	ds_read_b64_tr_b16 v[168:169], v210 offset:0x1200
	v_cvt_pk_f16_f32 v192, v144, v145
	v_exp_f32_e32 v143, v66
	v_mfma_f32_32x32x16_f16 v[96:111], a[200:203], a[168:171], v[96:111]
	ds_read_b64_tr_b16 v[170:171], v210 offset:0x1a00
	v_exp_f32_e32 v246, v67
	v_cvt_pk_f16_f32 v193, v146, v147
	v_mfma_f32_32x32x16_f16 v[48:63], a[232:235], a[136:139], v[48:63]
	ds_read_b64_tr_b16 v[160:161], v210 offset:0x1400
	v_exp_f32_e32 v247, v68
	v_exp_f32_e32 v248, v69
	v_cvt_pk_f16_f32 v194, v148, v149
	v_mfma_f32_32x32x16_f16 v[32:47], a[232:235], a[168:171], v[32:47]
	ds_read_b64_tr_b16 v[162:163], v210 offset:0x1c00
	ds_read_b64_tr_b16 v[136:137], v210 offset:0x1600
	v_exp_f32_e32 v249, v70
	v_exp_f32_e32 v250, v71
	v_cvt_pk_f16_f32 v195, v150, v151
	v_exp_f32_e32 v148, v72
	v_exp_f32_e32 v149, v73
	v_mfma_f32_32x32x16_f16 v[112:127], a[204:207], a[140:143], v[112:127]
	ds_read_b64_tr_b16 v[138:139], v210 offset:0x1e00
	v_cvt_pk_f16_f32 v144, v152, v153
	v_exp_f32_e32 v150, v74
	v_exp_f32_e32 v151, v75
	v_mfma_f32_32x32x16_f16 v[96:111], a[204:207], a[172:175], v[96:111]
	ds_read_b64_tr_b16 v[132:133], v210 offset:0x2000
	v_cvt_pk_f16_f32 v145, v154, v155
	v_exp_f32_e32 v152, v76
	v_exp_f32_e32 v153, v77
	v_mfma_f32_32x32x16_f16 v[48:63], a[236:239], a[140:143], v[48:63]
	ds_read_b64_tr_b16 v[134:135], v210 offset:0x2800
	v_cvt_pk_f16_f32 v146, v156, v157
	v_mfma_f32_32x32x16_f16 v[32:47], a[236:239], a[172:175], v[32:47]
	ds_read_b64_tr_b16 v[92:93], v210 offset:0x2200
	v_exp_f32_e32 v154, v78
	v_exp_f32_e32 v155, v79
	ds_read_b64_tr_b16 v[94:95], v210 offset:0x2a00
	v_cvt_pk_f16_f32 v147, v158, v159
	s_mov_b32 s0, s55
	v_mfma_f32_32x32x16_f16 v[112:127], a[208:211], a[144:147], v[112:127]
	ds_read_b64_tr_b16 v[88:89], v210 offset:0x2400
	v_cvt_pk_f16_f32 v84, v80, v81
	v_add_f32_e32 v64, v239, v80
	v_add_f32_e32 v65, v238, v81
	s_add_i32 s1, s31, 0x14000
	v_mfma_f32_32x32x16_f16 v[96:111], a[208:211], a[176:179], v[96:111]
	ds_read_b64_tr_b16 v[90:91], v210 offset:0x2c00
	v_cvt_pk_f16_f32 v85, v82, v83
	v_add_f32_e32 v64, v64, v82
	v_add_f32_e32 v65, v65, v83
	s_mov_b32 s34, s57
	v_mfma_f32_32x32x16_f16 v[48:63], a[240:243], a[144:147], v[48:63]
	ds_read_b64_tr_b16 v[80:81], v210 offset:0x2600
	v_cvt_pk_f16_f32 v86, v242, v243
	v_add_f32_e32 v64, v64, v242
	v_add_f32_e32 v65, v65, v243
	s_add_i32 s35, s31, 0x14400
	v_mfma_f32_32x32x16_f16 v[32:47], a[240:243], a[176:179], v[32:47]
	ds_read_b64_tr_b16 v[82:83], v210 offset:0x2e00
	ds_read_b64_tr_b16 v[76:77], v210 offset:0x3000
	v_cvt_pk_f16_f32 v87, v244, v245
	v_add_f32_e32 v64, v64, v244
	v_add_f32_e32 v65, v65, v245
	s_mov_b32 s91, s59
	v_mfma_f32_32x32x16_f16 v[112:127], a[212:215], a[148:151], v[112:127]
	ds_read_b64_tr_b16 v[78:79], v210 offset:0x3800
	v_add_f32_e32 v64, v64, v198
	v_add_f32_e32 v65, v65, v199
	s_add_i32 s92, s31, 0x14800
	v_mfma_f32_32x32x16_f16 v[96:111], a[212:215], a[180:183], v[96:111]
	ds_read_b64_tr_b16 v[72:73], v210 offset:0x3200
	v_add_f32_e32 v64, v64, v232
	v_add_f32_e32 v65, v65, v233
	s_mov_b32 s93, s61
	v_mfma_f32_32x32x16_f16 v[48:63], a[244:247], a[148:151], v[48:63]
	ds_read_b64_tr_b16 v[74:75], v210 offset:0x3a00
	v_add_f32_e32 v64, v64, v234
	v_add_f32_e32 v65, v65, v235
	s_add_i32 s94, s31, 0x14c00
	v_mfma_f32_32x32x16_f16 v[32:47], a[244:247], a[180:183], v[32:47]
	ds_read_b64_tr_b16 v[68:69], v210 offset:0x3400
	ds_read_b64_tr_b16 v[70:71], v210 offset:0x3c00
	v_add_f32_e32 v156, v64, v236
	v_add_f32_e32 v157, v65, v237
	s_mov_b32 s95, s38
	v_mfma_f32_32x32x16_f16 v[112:127], a[216:219], a[152:155], v[112:127]
	ds_read_b64_tr_b16 v[64:65], v210 offset:0x3600
	v_cvt_pk_f16_f32 v140, v141, v142
	v_add_f32_e32 v158, v240, v141
	v_add_f32_e32 v142, v241, v142
	v_mfma_f32_32x32x16_f16 v[96:111], a[216:219], a[184:187], v[96:111]
	ds_read_b64_tr_b16 v[66:67], v210 offset:0x3e00
	v_cvt_pk_f16_f32 v141, v143, v246
	v_add_f32_e32 v143, v158, v143
	v_add_f32_e32 v158, v142, v246
	v_mfma_f32_32x32x16_f16 v[48:63], a[248:251], a[152:155], v[48:63]
	s_mov_b32 s80, s63
	v_cvt_pk_f16_f32 v142, v247, v248
	v_add_f32_e32 v159, v143, v247
	v_add_f32_e32 v158, v158, v248
	v_mfma_f32_32x32x16_f16 v[32:47], a[248:251], a[184:187], v[32:47]
	s_add_i32 s96, s31, 0x10080
	v_cvt_pk_f16_f32 v143, v249, v250
	v_add_f32_e32 v159, v159, v249
	v_add_f32_e32 v158, v158, v250
	v_mfma_f32_32x32x16_f16 v[112:127], a[220:223], a[156:159], v[112:127]
	s_mov_b32 s97, s65
	v_add_f32_e32 v159, v159, v148
	v_add_f32_e32 v158, v158, v149
	v_mfma_f32_32x32x16_f16 v[96:111], a[220:223], a[188:191], v[96:111]
	v_add_f32_e32 v159, v159, v150
	v_add_f32_e32 v158, v158, v151
	v_mfma_f32_32x32x16_f16 v[48:63], a[252:255], a[156:159], v[48:63]
	s_mov_b32 s98, s66
	v_add_f32_e32 v159, v159, v152
	v_add_f32_e32 v158, v158, v153
	v_mfma_f32_32x32x16_f16 v[32:47], a[252:255], a[188:191], v[32:47]
	s_add_i32 s31, s31, 0x10880
	v_add_f32_e32 v159, v159, v154
	v_add_f32_e32 v158, v158, v155
	s_nop 4
	v_add_f32_e32 v156, v156, v157
	s_waitcnt vmcnt(0) lgkmcnt(0)
	s_barrier
	v_mov_b32_e32 v157, v156
	s_nop 1
	v_permlane32_swap_b32_e32 v156, v157
	v_add_f32_e32 v156, v156, v157
	v_add_f32_e32 v197, v197, v156
	v_add_f32_e32 v156, v159, v158
	v_mov_b32_e32 v157, v156
	s_nop 1
	v_permlane32_swap_b32_e32 v156, v157
	v_add_f32_e32 v156, v156, v157
	v_add_f32_e32 v196, v196, v156
	s_nop 1
	v_mfma_f32_32x32x16_f16 a[0:15], v[180:183], v[164:167], a[0:15]
	s_mov_b32 m0, s0
	s_nop 0
	buffer_load_dwordx4 v211, s[16:19], s1 offen lds
	v_mfma_f32_32x32x16_f16 a[16:31], v[180:183], v[192:195], a[16:31]
	s_mov_b32 m0, s34
	s_nop 0
	buffer_load_dwordx4 v212, s[16:19], s35 offen lds
	ds_read_b128 a[192:195], v206 offset:0
	v_mfma_f32_32x32x16_f16 a[32:47], v[184:187], v[164:167], a[32:47]
	s_mov_b32 m0, s91
	s_nop 0
	buffer_load_dwordx4 v211, s[16:19], s92 offen lds
	ds_read_b128 a[196:199], v207 offset:0
	v_mfma_f32_32x32x16_f16 a[48:63], v[184:187], v[192:195], a[48:63]
	s_mov_b32 m0, s93
	s_nop 0
	buffer_load_dwordx4 v212, s[16:19], s94 offen lds
	ds_read_b128 a[200:203], v208 offset:0
	v_mfma_f32_32x32x16_f16 a[64:79], v[176:179], v[164:167], a[64:79]
	s_mov_b32 m0, s95
	s_nop 0
	buffer_load_dwordx4 v213, s[20:23], s24 offen lds
	ds_read_b128 a[204:207], v209 offset:0
	v_mfma_f32_32x32x16_f16 a[80:95], v[176:179], v[192:195], a[80:95]
	s_mov_b32 m0, s80
	s_nop 0
	buffer_load_dwordx4 v213, s[20:23], s96 offen lds
	ds_read_b128 a[208:211], v206 offset:128
	v_mfma_f32_32x32x16_f16 a[96:111], v[188:191], v[164:167], a[96:111]
	s_mov_b32 m0, s97
	s_nop 0
	buffer_load_dwordx4 v213, s[20:23], s30 offen lds
	ds_read_b128 a[212:215], v207 offset:128
	v_mfma_f32_32x32x16_f16 a[112:127], v[188:191], v[192:195], a[112:127]
	s_mov_b32 m0, s98
	s_nop 0
	buffer_load_dwordx4 v213, s[20:23], s31 offen lds
	ds_read_b128 a[216:219], v208 offset:128
	v_mfma_f32_32x32x16_f16 a[0:15], v[172:175], v[128:131], a[0:15]
	ds_read_b128 a[220:223], v209 offset:128
	v_max3_f32 v156, v112, v113, v48
	v_max3_f32 v157, v114, v115, v49
	v_max3_f32 v156, v156, v50, v51
	v_mfma_f32_32x32x16_f16 a[16:31], v[172:175], v[144:147], a[16:31]
	ds_read_b128 a[224:227], v206 offset:8192
	v_max3_f32 v156, v156, v116, v117
	v_max3_f32 v157, v157, v118, v119
	v_max3_f32 v156, v156, v52, v53
	v_max3_f32 v157, v157, v54, v55
	v_mfma_f32_32x32x16_f16 a[32:47], v[168:171], v[128:131], a[32:47]
	ds_read_b128 a[228:231], v207 offset:8192
	v_max3_f32 v156, v156, v120, v121
	v_max3_f32 v157, v157, v122, v123
	v_max3_f32 v156, v156, v56, v57
	v_max3_f32 v157, v157, v58, v59
	v_mfma_f32_32x32x16_f16 a[48:63], v[168:171], v[144:147], a[48:63]
	ds_read_b128 a[232:235], v208 offset:8192
	v_max3_f32 v156, v156, v124, v125
	v_max3_f32 v157, v157, v126, v127
	v_max3_f32 v156, v156, v60, v61
	v_max3_f32 v157, v157, v62, v63
	v_mfma_f32_32x32x16_f16 a[64:79], v[160:163], v[128:131], a[64:79]
	ds_read_b128 a[236:239], v209 offset:8192
	v_max3_f32 v158, v96, v97, v32
	v_max3_f32 v159, v98, v99, v33
	v_max3_f32 v158, v158, v34, v35
	v_mfma_f32_32x32x16_f16 a[80:95], v[160:163], v[144:147], a[80:95]
	ds_read_b128 a[240:243], v206 offset:8320
	v_max3_f32 v158, v158, v100, v101
	v_max3_f32 v159, v159, v102, v103
	v_max3_f32 v158, v158, v36, v37
	v_max3_f32 v159, v159, v38, v39
	v_mfma_f32_32x32x16_f16 a[96:111], v[136:139], v[128:131], a[96:111]
	ds_read_b128 a[244:247], v207 offset:8320
	v_max3_f32 v128, v158, v104, v105
	v_max3_f32 v129, v159, v106, v107
	v_max3_f32 v128, v128, v40, v41
	v_max3_f32 v129, v129, v42, v43
	v_mfma_f32_32x32x16_f16 a[112:127], v[136:139], v[144:147], a[112:127]
	ds_read_b128 a[248:251], v208 offset:8320
	v_max3_f32 v128, v128, v108, v109
	v_max3_f32 v129, v129, v110, v111
	v_max3_f32 v128, v128, v44, v45
	v_max3_f32 v130, v129, v46, v47
	v_mfma_f32_32x32x16_f16 a[0:15], v[132:135], v[84:87], a[0:15]
	ds_read_b128 a[252:255], v209 offset:8320
	v_max_f32_e32 v129, v156, v157
	v_mov_b32_e32 v131, v129
	s_nop 1
	v_permlane32_swap_b32_e32 v129, v131
	v_max_f32_e32 v129, v129, v131
	v_mfma_f32_32x32x16_f16 a[16:31], v[132:135], v[140:143], a[16:31]
	v_max_f32_e32 v128, v128, v130
	v_mov_b32_e32 v130, v128
	s_nop 1
	v_permlane32_swap_b32_e32 v128, v130
	v_max_f32_e32 v128, v128, v130
	v_max_f32_e32 v130, v129, v129
	v_max_f32_e32 v131, v128, v128
	v_max_f32_e32 v130, v130, v131
	v_mfma_f32_32x32x16_f16 a[32:47], v[92:95], v[84:87], a[32:47]
	v_cmp_lt_f32_e32 vcc, s79, v130
	s_cmp_lg_u64 vcc, 0
	s_cselect_b64 s[0:1], -1, 0
	s_cbranch_vccnz .LBB3_19
.LBB3_15:
	v_cvt_pk_f16_f32 v156, v198, v199
	v_cvt_pk_f16_f32 v157, v232, v233
	v_cvt_pk_f16_f32 v158, v234, v235
	v_cvt_pk_f16_f32 v159, v236, v237
	v_cvt_pk_f16_f32 v160, v148, v149
	v_cvt_pk_f16_f32 v161, v150, v151
	v_cvt_pk_f16_f32 v162, v152, v153
	v_cvt_pk_f16_f32 v163, v154, v155
	v_exp_f32_e32 v128, v112
	v_exp_f32_e32 v129, v113
	v_mfma_f32_32x32x16_f16 a[48:63], v[92:95], v[140:143], a[48:63]
	v_exp_f32_e32 v130, v114
	v_exp_f32_e32 v131, v115
	v_mfma_f32_32x32x16_f16 a[64:79], v[88:91], v[84:87], a[64:79]
	v_add_f32_e32 v92, v201, v128
	v_add_f32_e32 v93, v201, v129
	v_exp_f32_e32 v132, v116
	v_exp_f32_e32 v133, v117
	v_exp_f32_e32 v134, v118
	v_mfma_f32_32x32x16_f16 a[80:95], v[88:91], v[140:143], a[80:95]
	v_add_f32_e32 v88, v92, v130
	v_add_f32_e32 v89, v93, v131
	v_exp_f32_e32 v135, v119
	v_exp_f32_e32 v136, v120
	v_mfma_f32_32x32x16_f16 a[96:111], v[80:83], v[84:87], a[96:111]
	v_add_f32_e32 v84, v88, v132
	v_add_f32_e32 v85, v89, v133
	v_add_f32_e32 v84, v84, v134
	v_exp_f32_e32 v137, v121
	v_exp_f32_e32 v138, v122
	v_exp_f32_e32 v139, v123
	v_mfma_f32_32x32x16_f16 a[112:127], v[80:83], v[140:143], a[112:127]
	v_add_f32_e32 v80, v85, v135
	v_add_f32_e32 v81, v84, v136
	v_exp_f32_e32 v140, v124
	v_exp_f32_e32 v141, v125
	v_mfma_f32_32x32x16_f16 a[0:15], v[76:79], v[156:159], a[0:15]
	v_add_f32_e32 v80, v80, v137
	v_add_f32_e32 v81, v81, v138
	v_add_f32_e32 v80, v80, v139
	v_exp_f32_e32 v142, v126
	v_exp_f32_e32 v143, v127
	v_exp_f32_e32 v144, v96
	v_mfma_f32_32x32x16_f16 a[16:31], v[76:79], v[160:163], a[16:31]
	v_add_f32_e32 v76, v81, v140
	v_add_f32_e32 v77, v80, v141
	v_exp_f32_e32 v145, v97
	v_exp_f32_e32 v146, v98
	v_mfma_f32_32x32x16_f16 a[32:47], v[72:75], v[156:159], a[32:47]
	v_add_f32_e32 v241, v76, v142
	v_add_f32_e32 v240, v77, v143
	v_add_f32_e32 v76, v201, v144
	v_exp_f32_e32 v147, v99
	v_exp_f32_e32 v148, v100
	v_exp_f32_e32 v149, v101
	v_mfma_f32_32x32x16_f16 a[48:63], v[72:75], v[160:163], a[48:63]
	v_add_f32_e32 v72, v201, v145
	v_add_f32_e32 v73, v76, v146
	v_exp_f32_e32 v150, v102
	v_exp_f32_e32 v151, v103
	v_mfma_f32_32x32x16_f16 a[64:79], v[68:71], v[156:159], a[64:79]
	v_add_f32_e32 v72, v72, v147
	v_add_f32_e32 v73, v73, v148
	v_add_f32_e32 v72, v72, v149
	v_exp_f32_e32 v152, v104
	v_exp_f32_e32 v153, v105
	v_exp_f32_e32 v154, v106
	v_mfma_f32_32x32x16_f16 a[80:95], v[68:71], v[160:163], a[80:95]
	v_add_f32_e32 v68, v73, v150
	v_add_f32_e32 v69, v72, v151
	v_mfma_f32_32x32x16_f16 a[96:111], v[64:67], v[156:159], a[96:111]
	v_exp_f32_e32 v155, v107
	v_exp_f32_e32 v156, v108
	v_add_f32_e32 v68, v68, v152
	v_add_f32_e32 v69, v69, v153
	v_add_f32_e32 v68, v68, v154
	v_exp_f32_e32 v157, v109
	v_exp_f32_e32 v158, v110
	v_exp_f32_e32 v159, v111
	v_mfma_f32_32x32x16_f16 a[112:127], v[64:67], v[160:163], a[112:127]
	v_add_f32_e32 v64, v69, v155
	v_add_f32_e32 v65, v68, v156
	s_andn2_b64 vcc, exec, s[0:1]
	v_add_f32_e32 v64, v64, v157
	v_add_f32_e32 v242, v65, v158
	s_nop 0
	v_add_f32_e32 v243, v64, v159
	s_cbranch_vccz .LBB3_20
